# speedup vs baseline: 1.0209x; 1.0157x over previous
_Z12giou_partialPK15HIP_vector_typeIfLj4EES2_S2_PKiPS_IfLj2EE:
	s_cmpk_ge_u32 s2, 0x100
	s_cbranch_scc1 .Llate_block
	s_setprio 3
	s_load_dwordx8 s[16:23], s[0:1], 0x0
	s_load_dwordx2 s[24:25], s[0:1], 0x20
	s_movk_i32 s3, 0x200
	s_lshl_b32 s6, s2, 10
	v_cmp_gt_u32_e32 vcc, s3, v0
	v_lshlrev_b32_e32 v11, 4, v0
	v_lshrrev_b32_e32 v1, 6, v0
	v_and_b32_e32 v10, 63, v0
	v_lshl_add_u32 v6, v1, 18, s6
	v_lshlrev_b32_e32 v8, 2, v6
	v_lshl_add_u32 v8, v10, 4, v8
	s_lshl_b32 s7, s2, 14
	v_readfirstlane_b32 s15, v1
	v_add_u32_e32 v43, 0x200, v6
	s_waitcnt lgkmcnt(0)
	s_add_u32 s20, s20, s7
	s_addc_u32 s21, s21, 0
	global_load_dwordx4 v[12:15], v8, s[22:23] nt
	global_load_dwordx4 v[16:19], v8, s[22:23] offset:1024 nt
	global_load_dwordx4 v[26:29], v8, s[22:23] offset:2048 nt
	global_load_dwordx4 v[30:33], v8, s[22:23] offset:3072 nt
	s_and_saveexec_b64 s[8:9], vcc
	s_cbranch_execz .Lno_anc
	v_add_u32_e32 v9, 0x2000, v11
	global_load_dwordx4 v[2:5], v11, s[20:21] nt
	global_load_dwordx4 v[44:47], v9, s[20:21] nt

.Llate_block:
	v_cmp_eq_u32_e32 vcc, 0, v0
	s_and_saveexec_b64 s[4:5], vcc
	s_cbranch_execz .Llate_end
	s_load_dwordx2 s[24:25], s[0:1], 0x20
	s_lshl_b32 s6, s2, 3
	v_mov_b32_e32 v2, 0
	v_mov_b32_e32 v3, 0
	v_mov_b32_e32 v4, s6
	s_waitcnt lgkmcnt(0)
	global_store_dwordx2 v4, v[2:3], s[24:25]
